# P0-P1 barrier: norm weights and the first x row of each wave loaded while the wave waits at the barrier's final s_barrier
# speedup vs baseline: 1.0050x; 1.0050x over previous
.LBB0_73:
	s_or_b64 exec, exec, s[2:3]
	v_lshlrev_b32_e32 v132, 4, v178
	v_and_b32_e32 v134, 0x3f0, v132
	v_add_u32_e32 v135, 0x1000, v134
	global_load_dwordx4 v[2:5], v134, s[12:13]
	global_load_dwordx4 v[6:9], v134, s[12:13] offset:1024
	global_load_dwordx4 v[10:13], v134, s[12:13] offset:2048
	global_load_dwordx4 v[14:17], v134, s[12:13] offset:3072
	global_load_dwordx4 v[18:21], v135, s[12:13]
	global_load_dwordx4 v[22:25], v135, s[12:13] offset:1024
	global_load_dwordx4 v[26:29], v135, s[12:13] offset:2048
	global_load_dwordx4 v[30:33], v135, s[12:13] offset:3072
	v_lshrrev_b32_e32 v132, 6, v178
	v_lshl_add_u32 v132, s33, 3, v132
	v_mov_b32_e32 v133, 0
	v_lshlrev_b64 v[132:133], 13, v[132:133]
	v_lshl_add_u64 v[132:133], s[8:9], 0, v[132:133]
	v_mov_b32_e32 v135, 0
	v_lshl_add_u64 v[132:133], v[132:133], 0, v[134:135]
	s_mov_b64 s[100:101], 0x1000
	v_lshl_add_u64 v[132:133], v[132:133], 0, s[100:101]
	global_load_dwordx4 v[100:103], v[132:133], off
	global_load_dwordx4 v[104:107], v[132:133], off offset:1024
	global_load_dwordx4 v[108:111], v[132:133], off offset:2048
	global_load_dwordx4 v[112:115], v[132:133], off offset:3072
	global_load_dwordx4 v[116:119], v[132:133], off offset:-4096
	global_load_dwordx4 v[120:123], v[132:133], off offset:-3072
	global_load_dwordx4 v[124:127], v[132:133], off offset:-2048
	global_load_dwordx4 v[128:131], v[132:133], off offset:-1024
	s_barrier
.LBB0_74:
	s_cmp_lt_i32 s94, 2
	s_cselect_b64 s[2:3], -1, 0
	s_and_b64 s[0:1], s[2:3], s[0:1]
	s_andn2_b64 vcc, exec, s[0:1]
	v_lshrrev_b32_e32 v179, 6, v178
	s_cbranch_vccnz .LBB0_79
	v_lshl_add_u32 v66, s33, 3, v179
	s_waitcnt lgkmcnt(0)
	s_movk_i32 s16, 0x2000
	v_cmp_gt_i32_e32 vcc, s16, v66
	s_and_saveexec_b64 s[2:3], vcc
	s_cbranch_execz .LBB0_78
	v_lshlrev_b32_e32 v1, 4, v178
	v_and_b32_e32 v34, 0x3f0, v1
	v_mov_b32_e32 v35, 0
	s_movk_i32 s17, 0x1000
	v_mbcnt_lo_u32_b32 v1, -1, 0
	v_lshl_add_u64 v[68:69], s[92:93], 0, v[34:35]
	v_mbcnt_hi_u32_b32 v34, -1, v1
	v_and_b32_e32 v1, 64, v34
	v_add_u32_e32 v35, 64, v1
	v_xor_b32_e32 v1, 32, v34
	v_cmp_lt_i32_e32 vcc, v1, v35
	v_xor_b32_e32 v36, 16, v34
	v_ashrrev_i32_e32 v67, 31, v66
	v_cndmask_b32_e32 v1, v34, v1, vcc
	v_cmp_lt_i32_e32 vcc, v36, v35
	s_mov_b64 s[6:7], 0x1000
	s_lshl_b32 s4, s96, 3
	v_cndmask_b32_e32 v36, v34, v36, vcc
	v_lshlrev_b32_e32 v74, 2, v36
	v_xor_b32_e32 v36, 8, v34
	v_cmp_lt_i32_e32 vcc, v36, v35
	s_ashr_i32 s5, s4, 31
	s_mov_b64 s[10:11], 0x40000
	v_cndmask_b32_e32 v36, v34, v36, vcc
	v_lshlrev_b32_e32 v75, 2, v36
	v_xor_b32_e32 v36, 4, v34
	v_cmp_lt_i32_e32 vcc, v36, v35
	v_lshlrev_b32_e32 v1, 2, v1
	s_mov_b64 s[12:13], 0
	v_cndmask_b32_e32 v36, v34, v36, vcc
	v_lshlrev_b32_e32 v76, 2, v36
	v_xor_b32_e32 v36, 2, v34
	v_cmp_lt_i32_e32 vcc, v36, v35
	s_mov_b32 s18, 0x800000
	s_movk_i32 s19, 0x1fff
	v_cndmask_b32_e32 v36, v34, v36, vcc
	v_lshlrev_b32_e32 v77, 2, v36
	v_xor_b32_e32 v36, 1, v34
	v_cmp_lt_i32_e32 vcc, v36, v35
	s_nop 1
	v_cndmask_b32_e32 v34, v34, v36, vcc
	v_lshlrev_b32_e32 v78, 2, v34
	v_lshlrev_b64 v[34:35], 13, v[66:67]
	v_and_b32_e32 v36, 63, v178
	v_lshl_or_b32 v34, v36, 4, v34
	v_lshl_add_u64 v[34:35], s[8:9], 0, v[34:35]
	v_lshl_add_u64 v[70:71], v[34:35], 0, s[6:7]
	v_lshlrev_b64 v[34:35], 12, v[66:67]
	v_lshl_or_b32 v34, v36, 3, v34
	v_lshl_add_u64 v[34:35], s[90:91], 0, v[34:35]
	s_lshl_b64 s[6:7], s[4:5], 13
	v_lshl_add_u64 v[72:73], v[34:35], 0, s[10:11]
	s_lshl_b64 s[10:11], s[4:5], 12
	s_movk_i32 s5, 0x3000
	v_mov_b32_e32 v67, 0x358637bd
	s_waitcnt vmcnt(0)
	v_mov_b64_e32 v[38:39], v[100:101]
	v_mov_b64_e32 v[40:41], v[102:103]
	v_mov_b64_e32 v[34:35], v[104:105]
	v_mov_b64_e32 v[36:37], v[106:107]
	v_mov_b64_e32 v[46:47], v[108:109]
	v_mov_b64_e32 v[48:49], v[110:111]
	v_mov_b64_e32 v[42:43], v[112:113]
	v_mov_b64_e32 v[44:45], v[114:115]
	v_mov_b64_e32 v[50:51], v[116:117]
	v_mov_b64_e32 v[52:53], v[118:119]
	v_mov_b64_e32 v[54:55], v[120:121]
	v_mov_b64_e32 v[56:57], v[122:123]
	v_mov_b64_e32 v[62:63], v[124:125]
	v_mov_b64_e32 v[64:65], v[126:127]
	v_mov_b64_e32 v[58:59], v[128:129]
	v_mov_b64_e32 v[60:61], v[130:131]
	s_branch .Lp1_have_row

.Lp1_have_row:
	v_ashrrev_i32_e32 v79, 31, v66
	v_lshrrev_b32_e32 v79, 21, v79
	v_add_u32_e32 v79, v66, v79
	v_ashrrev_i32_e32 v79, 11, v79
	v_mul_i32_i24_e32 v80, 0x3000, v79
	v_add_u32_e32 v66, s4, v66
	v_ashrrev_i32_e32 v81, 31, v80
	v_cmp_lt_i32_e32 vcc, s19, v66
	v_lshl_add_u64 v[92:93], v[80:81], 2, v[68:69]
	s_or_b64 s[12:13], vcc, s[12:13]
	v_add_co_u32_e32 v124, vcc, s5, v92
	global_load_dwordx4 v[80:83], v[92:93], off
	global_load_dwordx4 v[84:87], v[92:93], off offset:1024
	v_addc_co_u32_e32 v125, vcc, 0, v93, vcc
	v_add_co_u32_e32 v140, vcc, s17, v92
	v_lshl_add_u64 v[70:71], v[70:71], 0, s[6:7]
	s_nop 0
	v_addc_co_u32_e32 v141, vcc, 0, v93, vcc
	v_add_co_u32_e32 v108, vcc, s16, v92
	s_waitcnt vmcnt(9)
	v_mov_b32_e32 v146, v39
	v_addc_co_u32_e32 v109, vcc, 0, v93, vcc
	global_load_dwordx4 v[88:91], v[92:93], off offset:2048
	s_nop 0
	global_load_dwordx4 v[92:95], v[92:93], off offset:3072
	s_nop 0
	global_load_dwordx4 v[96:99], v[124:125], off offset:-4096
	global_load_dwordx4 v[100:103], v[108:109], off offset:1024
	global_load_dwordx4 v[104:107], v[108:109], off offset:2048
	s_nop 0
	global_load_dwordx4 v[108:111], v[108:109], off offset:3072
	s_nop 0
	global_load_dwordx4 v[112:115], v[124:125], off
	global_load_dwordx4 v[116:119], v[124:125], off offset:1024
	global_load_dwordx4 v[120:123], v[124:125], off offset:2048
	s_nop 0
	global_load_dwordx4 v[124:127], v[124:125], off offset:3072
	s_nop 0
	global_load_dwordx4 v[128:131], v[140:141], off offset:3072
	global_load_dwordx4 v[132:135], v[140:141], off
	global_load_dwordx4 v[136:139], v[140:141], off offset:1024
	s_nop 0
	global_load_dwordx4 v[140:143], v[140:141], off offset:2048
	s_waitcnt vmcnt(19)
	v_mul_f32_e32 v79, v51, v51
	s_waitcnt vmcnt(18)
	v_mul_f32_e32 v160, v55, v55
	s_waitcnt vmcnt(17)
	v_mul_f32_e32 v161, v63, v63
	v_fmac_f32_e32 v79, v50, v50
	v_fmac_f32_e32 v160, v54, v54
	v_mov_b32_e32 v147, v35
	s_waitcnt vmcnt(16)
	v_mul_f32_e32 v162, v59, v59
	v_fmac_f32_e32 v161, v62, v62
	v_fmac_f32_e32 v79, v52, v52
	v_fmac_f32_e32 v160, v56, v56
	v_mov_b32_e32 v144, v38
	v_mov_b32_e32 v145, v34
	v_pk_mul_f32 v[146:147], v[146:147], v[146:147]
	v_fmac_f32_e32 v162, v58, v58
	v_fmac_f32_e32 v161, v64, v64
	v_fmac_f32_e32 v79, v53, v53
	v_fmac_f32_e32 v160, v57, v57
	v_mov_b32_e32 v148, v40
	v_mov_b32_e32 v149, v36
	v_mov_b32_e32 v152, v47
	v_mov_b32_e32 v153, v43
	v_pk_fma_f32 v[144:145], v[144:145], v[144:145], v[146:147]
	v_fmac_f32_e32 v162, v60, v60
	v_fmac_f32_e32 v161, v65, v65
	v_add_f32_e32 v79, v79, v160
	v_mov_b32_e32 v150, v46
	v_mov_b32_e32 v151, v42
	v_mov_b32_e32 v154, v41
	v_mov_b32_e32 v155, v37
	v_pk_mul_f32 v[152:153], v[152:153], v[152:153]
	v_pk_fma_f32 v[144:145], v[148:149], v[148:149], v[144:145]
	v_fmac_f32_e32 v162, v61, v61
	v_add_f32_e32 v79, v79, v161
	v_mov_b32_e32 v156, v48
	v_mov_b32_e32 v157, v44
	v_pk_fma_f32 v[146:147], v[150:151], v[150:151], v[152:153]
	v_pk_fma_f32 v[144:145], v[154:155], v[154:155], v[144:145]
	v_add_f32_e32 v79, v79, v162
	v_mov_b32_e32 v158, v49
	v_mov_b32_e32 v159, v45
	v_pk_fma_f32 v[146:147], v[156:157], v[156:157], v[146:147]
	v_add_f32_e32 v79, v79, v144
	v_pk_fma_f32 v[146:147], v[158:159], v[158:159], v[146:147]
	v_add_f32_e32 v79, v79, v145
	v_add_f32_e32 v79, v79, v146
	v_add_f32_e32 v79, v79, v147
	ds_bpermute_b32 v144, v1, v79
	s_waitcnt lgkmcnt(0)
	v_add_f32_e32 v79, v79, v144
	ds_bpermute_b32 v144, v74, v79
	s_waitcnt lgkmcnt(0)
	v_add_f32_e32 v79, v79, v144
	ds_bpermute_b32 v144, v75, v79
	s_waitcnt lgkmcnt(0)
	v_add_f32_e32 v79, v79, v144
	ds_bpermute_b32 v144, v76, v79
	s_waitcnt vmcnt(11)
	v_pk_add_f32 v[98:99], v[98:99], 1.0 op_sel_hi:[1,0]
	s_waitcnt lgkmcnt(0)
	v_add_f32_e32 v79, v79, v144
	ds_bpermute_b32 v144, v77, v79
	v_pk_add_f32 v[96:97], v[96:97], 1.0 op_sel_hi:[1,0]
	s_waitcnt vmcnt(10)
	v_pk_add_f32 v[102:103], v[102:103], 1.0 op_sel_hi:[1,0]
	v_pk_add_f32 v[100:101], v[100:101], 1.0 op_sel_hi:[1,0]
	s_waitcnt vmcnt(9)
	v_pk_add_f32 v[106:107], v[106:107], 1.0 op_sel_hi:[1,0]
	s_waitcnt lgkmcnt(0)
	v_add_f32_e32 v79, v79, v144
	ds_bpermute_b32 v144, v78, v79
	v_pk_add_f32 v[104:105], v[104:105], 1.0 op_sel_hi:[1,0]
	s_waitcnt vmcnt(8)
	v_pk_add_f32 v[110:111], v[110:111], 1.0 op_sel_hi:[1,0]
	v_pk_add_f32 v[108:109], v[108:109], 1.0 op_sel_hi:[1,0]
	s_waitcnt vmcnt(7)
	v_pk_add_f32 v[114:115], v[114:115], 1.0 op_sel_hi:[1,0]
	s_waitcnt lgkmcnt(0)
	v_add_f32_e32 v79, v79, v144
	v_fmamk_f32 v79, v79, 0x3a000000, v67
	v_mul_f32_e32 v144, 0x4b800000, v79
	v_cmp_gt_f32_e32 vcc, s18, v79
	v_pk_add_f32 v[112:113], v[112:113], 1.0 op_sel_hi:[1,0]
	s_waitcnt vmcnt(6)
	v_pk_add_f32 v[118:119], v[118:119], 1.0 op_sel_hi:[1,0]
	v_cndmask_b32_e32 v79, v79, v144, vcc
	v_rsq_f32_e32 v79, v79
	v_pk_add_f32 v[116:117], v[116:117], 1.0 op_sel_hi:[1,0]
	s_waitcnt vmcnt(5)
	v_pk_add_f32 v[122:123], v[122:123], 1.0 op_sel_hi:[1,0]
	v_pk_add_f32 v[120:121], v[120:121], 1.0 op_sel_hi:[1,0]
	v_mul_f32_e32 v144, 0x45800000, v79
	v_cndmask_b32_e32 v144, v79, v144, vcc
	v_pk_mul_f32 v[52:53], v[52:53], v[144:145] op_sel_hi:[1,0]
	v_pk_mul_f32 v[50:51], v[50:51], v[144:145] op_sel_hi:[1,0]
	v_pk_mul_f32 v[56:57], v[56:57], v[144:145] op_sel_hi:[1,0]
	v_pk_mul_f32 v[54:55], v[54:55], v[144:145] op_sel_hi:[1,0]
	v_pk_mul_f32 v[64:65], v[64:65], v[144:145] op_sel_hi:[1,0]
	v_pk_mul_f32 v[62:63], v[62:63], v[144:145] op_sel_hi:[1,0]
	v_pk_mul_f32 v[60:61], v[60:61], v[144:145] op_sel_hi:[1,0]
	v_pk_mul_f32 v[58:59], v[58:59], v[144:145] op_sel_hi:[1,0]
	v_pk_mul_f32 v[40:41], v[40:41], v[144:145] op_sel_hi:[1,0]
	v_pk_mul_f32 v[38:39], v[38:39], v[144:145] op_sel_hi:[1,0]
	v_pk_mul_f32 v[36:37], v[36:37], v[144:145] op_sel_hi:[1,0]
	v_pk_mul_f32 v[34:35], v[34:35], v[144:145] op_sel_hi:[1,0]
	v_pk_mul_f32 v[48:49], v[48:49], v[144:145] op_sel_hi:[1,0]
	v_pk_mul_f32 v[46:47], v[46:47], v[144:145] op_sel_hi:[1,0]
	v_pk_mul_f32 v[44:45], v[44:45], v[144:145] op_sel_hi:[1,0]
	v_pk_mul_f32 v[42:43], v[42:43], v[144:145] op_sel_hi:[1,0]
	v_pk_mul_f32 v[52:53], v[4:5], v[52:53]
	v_pk_mul_f32 v[50:51], v[2:3], v[50:51]
	s_waitcnt vmcnt(4)
	v_pk_add_f32 v[126:127], v[126:127], 1.0 op_sel_hi:[1,0]
	v_pk_add_f32 v[124:125], v[124:125], 1.0 op_sel_hi:[1,0]
	v_pk_mul_f32 v[56:57], v[8:9], v[56:57]
	v_pk_mul_f32 v[54:55], v[6:7], v[54:55]
	v_pk_mul_f32 v[64:65], v[12:13], v[64:65]
	v_pk_mul_f32 v[62:63], v[10:11], v[62:63]
	v_pk_mul_f32 v[60:61], v[16:17], v[60:61]
	v_pk_mul_f32 v[58:59], v[14:15], v[58:59]
	v_pk_mul_f32 v[40:41], v[20:21], v[40:41]
	v_pk_mul_f32 v[38:39], v[18:19], v[38:39]
	v_pk_mul_f32 v[36:37], v[24:25], v[36:37]
	v_pk_mul_f32 v[34:35], v[22:23], v[34:35]
	v_pk_mul_f32 v[48:49], v[28:29], v[48:49]
	v_pk_mul_f32 v[46:47], v[26:27], v[46:47]
	v_pk_mul_f32 v[44:45], v[32:33], v[44:45]
	v_pk_mul_f32 v[42:43], v[30:31], v[42:43]
	v_pk_fma_f32 v[52:53], v[98:99], v[52:53], v[82:83]
	v_pk_fma_f32 v[50:51], v[96:97], v[50:51], v[80:81]
	v_pk_fma_f32 v[56:57], v[102:103], v[56:57], v[86:87]
	v_pk_fma_f32 v[54:55], v[100:101], v[54:55], v[84:85]
	v_pk_fma_f32 v[64:65], v[106:107], v[64:65], v[90:91]
	v_pk_fma_f32 v[62:63], v[104:105], v[62:63], v[88:89]
	v_pk_fma_f32 v[60:61], v[110:111], v[60:61], v[94:95]
	v_pk_fma_f32 v[58:59], v[108:109], v[58:59], v[92:93]
	s_waitcnt vmcnt(2)
	v_pk_fma_f32 v[40:41], v[114:115], v[40:41], v[134:135]
	v_pk_fma_f32 v[38:39], v[112:113], v[38:39], v[132:133]
	s_waitcnt vmcnt(1)
	v_pk_fma_f32 v[36:37], v[36:37], v[118:119], v[138:139]
	v_pk_fma_f32 v[34:35], v[34:35], v[116:117], v[136:137]
	s_waitcnt vmcnt(0)
	v_pk_fma_f32 v[48:49], v[48:49], v[122:123], v[142:143]
	v_pk_fma_f32 v[46:47], v[46:47], v[120:121], v[140:141]
	v_pk_fma_f32 v[44:45], v[44:45], v[126:127], v[130:131]
	v_pk_fma_f32 v[42:43], v[42:43], v[124:125], v[128:129]
	v_cvt_pk_bf16_f32 v50, v50, v51
	v_cvt_pk_bf16_f32 v51, v52, v53
	v_cvt_pk_bf16_f32 v52, v54, v55
	v_cvt_pk_bf16_f32 v53, v56, v57
	v_cvt_pk_bf16_f32 v54, v62, v63
	v_cvt_pk_bf16_f32 v55, v64, v65
	v_cvt_pk_bf16_f32 v56, v58, v59
	v_cvt_pk_bf16_f32 v57, v60, v61
	v_cvt_pk_bf16_f32 v38, v38, v39
	v_cvt_pk_bf16_f32 v39, v40, v41
	v_cvt_pk_bf16_f32 v34, v34, v35
	v_cvt_pk_bf16_f32 v35, v36, v37
	v_cvt_pk_bf16_f32 v36, v46, v47
	v_cvt_pk_bf16_f32 v37, v48, v49
	v_cvt_pk_bf16_f32 v40, v42, v43
	v_cvt_pk_bf16_f32 v41, v44, v45
	global_store_dwordx2 v[72:73], v[50:51], off
	global_store_dwordx2 v[72:73], v[52:53], off offset:512
	global_store_dwordx2 v[72:73], v[54:55], off offset:1024
	global_store_dwordx2 v[72:73], v[56:57], off offset:1536
	global_store_dwordx2 v[72:73], v[38:39], off offset:2048
	global_store_dwordx2 v[72:73], v[34:35], off offset:2560
	global_store_dwordx2 v[72:73], v[36:37], off offset:3072
	global_store_dwordx2 v[72:73], v[40:41], off offset:3584
	v_lshl_add_u64 v[72:73], v[72:73], 0, s[10:11]
	s_andn2_b64 exec, exec, s[12:13]
	s_cbranch_execnz .LBB0_77
